# speedup vs baseline: 1.0053x; 1.0053x over previous
.LBB1_12:
	s_mov_b32 s0, s44
	s_add_i32 s44, s44, 1
	s_cmp_ge_u32 s44, s42
	s_cselect_b64 s[22:23], -1, 0
	s_cmp_lt_u32 s44, s42
	s_cselect_b32 s2, s44, s0
	s_waitcnt vmcnt(0)
	s_lshl_b32 s0, s2, 4
	s_mov_b32 s1, s17
	s_mov_b32 m0, s43
	ds_read_b128 v[76:79], v119 offset:32768
	ds_read_b128 v[80:83], v119 offset:36864
	ds_read_b128 v[84:87], v120 offset:32768
	ds_read_b128 v[88:91], v120 offset:36864
	ds_read_b128 v[92:95], v121
	ds_read_b128 v[96:99], v121 offset:4096
	ds_read_b128 v[128:131], v122
	ds_read_b128 v[132:135], v122 offset:4096
	ds_read_b128 v[72:75], v123
	s_waitcnt lgkmcnt(0)
	v_lshl_add_u64 v[70:71], s[0:1], 2, v[2:3]
	global_load_lds_dword v[70:71], off
	ds_read_b128 v[156:159], v115
	ds_read_b128 v[160:163], v115 offset:1024
	ds_read_b128 v[164:167], v115 offset:2048
	v_cvt_pk_bf16_f32 v136, v76, v77
	v_cvt_pk_bf16_f32 v137, v78, v79
	v_cvt_pk_bf16_f32 v138, v84, v85
	v_cvt_pk_bf16_f32 v139, v86, v87
	v_cvt_pk_bf16_f32 v140, v92, v93
	v_cvt_pk_bf16_f32 v141, v94, v95
	v_cvt_pk_bf16_f32 v142, v128, v129
	v_cvt_pk_bf16_f32 v143, v130, v131
	v_cvt_pk_bf16_f32 v144, v80, v81
	v_cvt_pk_bf16_f32 v145, v82, v83
	v_cvt_pk_bf16_f32 v146, v88, v89
	v_cvt_pk_bf16_f32 v147, v90, v91
	v_cvt_pk_bf16_f32 v128, v96, v97
	v_cvt_pk_bf16_f32 v129, v98, v99
	v_cvt_pk_bf16_f32 v130, v132, v133
	v_cvt_pk_bf16_f32 v131, v134, v135
	s_lshl_b32 s0, s2, 13
	s_cmp_lt_u32 s44, s42
	s_cselect_b32 s0, s0, 0x1e848000
	s_mov_b32 s61, s0
	s_add_i32 s63, s44, 1
	s_cmp_eq_u32 s63, s42
	s_cselect_b32 s63, 1, 0
	s_nop 0
	s_nop 0
	s_nop 0
	s_nop 0
	s_nop 0
	s_nop 0
	s_nop 0
	s_nop 0
	ds_read_b128 v[132:135], v115 offset:3072
	s_waitcnt lgkmcnt(3)
	v_mfma_f32_16x16x32_bf16 v[148:151], v[136:139], v[156:159], v[36:39]
	ds_read_b128 v[156:159], v115 offset:4096
	s_waitcnt lgkmcnt(3)
	v_mfma_f32_16x16x32_bf16 v[152:155], v[136:139], v[160:163], v[40:43]
	ds_read_b128 v[160:163], v115 offset:5120
	s_waitcnt lgkmcnt(3)
	v_mfma_f32_16x16x32_bf16 v[96:99], v[136:139], v[164:167], v[44:47]
	ds_read_b128 v[164:167], v115 offset:6144
	s_waitcnt lgkmcnt(3)
	v_mfma_f32_16x16x32_bf16 v[92:95], v[136:139], v[132:135], v[48:51]
	ds_read_b128 v[132:135], v115 offset:7168
	s_waitcnt lgkmcnt(3)
	v_mfma_f32_16x16x32_bf16 v[88:91], v[136:139], v[156:159], v[52:55]
	ds_read_b128 v[156:159], v115 offset:8192
	s_waitcnt lgkmcnt(3)
	v_mfma_f32_16x16x32_bf16 v[84:87], v[136:139], v[160:163], v[56:59]
	ds_read_b128 v[160:163], v115 offset:9216
	s_waitcnt lgkmcnt(3)
	v_mfma_f32_16x16x32_bf16 v[80:83], v[136:139], v[164:167], v[60:63]
	ds_read_b128 v[164:167], v115 offset:10240
	s_waitcnt lgkmcnt(3)
	v_mfma_f32_16x16x32_bf16 v[76:79], v[136:139], v[132:135], v[64:67]
	ds_read_b128 v[132:135], v115 offset:11264
	s_waitcnt lgkmcnt(3)
	v_mfma_f32_16x16x32_bf16 v[148:151], v[140:143], v[156:159], v[148:151]
	ds_read_b128 v[156:159], v115 offset:12288
	s_waitcnt lgkmcnt(3)
	v_mfma_f32_16x16x32_bf16 v[152:155], v[140:143], v[160:163], v[152:155]
	ds_read_b128 v[160:163], v115 offset:13312
	s_waitcnt lgkmcnt(3)
	v_mfma_f32_16x16x32_bf16 v[96:99], v[140:143], v[164:167], v[96:99]
	ds_read_b128 v[164:167], v115 offset:14336
	s_waitcnt lgkmcnt(3)
	v_mfma_f32_16x16x32_bf16 v[92:95], v[140:143], v[132:135], v[92:95]
	ds_read_b128 v[132:135], v115 offset:15360
	s_waitcnt lgkmcnt(3)
	v_mfma_f32_16x16x32_bf16 v[88:91], v[140:143], v[156:159], v[88:91]
	ds_read_b128 v[156:159], v115 offset:16384
	s_waitcnt lgkmcnt(3)
	v_mfma_f32_16x16x32_bf16 v[84:87], v[140:143], v[160:163], v[84:87]
	ds_read_b128 v[160:163], v115 offset:17408
	s_waitcnt lgkmcnt(3)
	v_mfma_f32_16x16x32_bf16 v[80:83], v[140:143], v[164:167], v[80:83]
	ds_read_b128 v[164:167], v115 offset:18432
	s_waitcnt lgkmcnt(3)
	v_mfma_f32_16x16x32_bf16 v[76:79], v[140:143], v[132:135], v[76:79]
	ds_read_b128 v[132:135], v115 offset:19456
	s_waitcnt lgkmcnt(3)
	s_mov_b32 m0, s47
	s_nop 0
	buffer_load_dwordx4 v113, s[12:15], s61 offen nt lds
	s_cmp_eq_u32 s63, 0
	s_cbranch_scc1 .Lmain_noburst
	s_or_b32 s62, s61, 0x800
	s_mov_b32 m0, s48
	s_nop 0
	buffer_load_dwordx4 v113, s[12:15], s62 offen nt lds
	s_or_b32 s62, s61, 0x1000
	s_mov_b32 m0, s49
	s_nop 0
	buffer_load_dwordx4 v113, s[12:15], s62 offen nt lds
	s_or_b32 s62, s61, 0x1800
	s_mov_b32 m0, s50
	s_nop 0
	buffer_load_dwordx4 v113, s[12:15], s62 offen nt lds
	s_or_b32 s62, s61, 0x100
	s_mov_b32 m0, s51
	s_nop 0
	buffer_load_dwordx4 v113, s[12:15], s62 offen nt lds
	s_or_b32 s62, s61, 0x900
	s_mov_b32 m0, s52
	s_nop 0
	buffer_load_dwordx4 v113, s[12:15], s62 offen nt lds
	s_or_b32 s62, s61, 0x1100
	s_mov_b32 m0, s53
	s_nop 0
	buffer_load_dwordx4 v113, s[12:15], s62 offen nt lds
	s_or_b32 s62, s61, 0x1900
	s_mov_b32 m0, s54
	s_nop 0
	buffer_load_dwordx4 v113, s[12:15], s62 offen nt lds
